# gqa16 tile loop: all 16 bf16 packs of P in the K-read latency gap behind the barrier instead of behind Q.K MFMAs
# baseline (speedup 1.0000x reference)
; #define SBAR() __builtin_amdgcn_sched_barrier(0)
; template <int LDQ, int LDK, int LDO>
; __device__ __forceinline__ void attn_gqa16_body(const bf16* __restrict__ Qb, const bf16* __restrict__ Kh, const bf16* __restrict__ Vh, bf16* __restrict__ Ob, int seq, char* lds, float mref) {
;     ...
;   for (int t = 0; t < NT; ++t) {
;     HPACK();
;     __syncthreads();
;     const bool more = t + 1 < NT;
;     if (more) HQK((t + 1) & 1);
;     const int vb = vb0 + (t & 1) * (int)G16_V;
;     SBAR(); pv16<0>(o, vb, pb); SBAR();
.LBB0_650:
	s_add_i32 s17, s16, 1
	s_and_b32 s16, s16, 1
	s_and_b32 s46, 1, s17
	s_cmp_eq_u32 s46, 1
	s_cselect_b32 s85, s86, s84
	s_cselect_b32 s46, 0x4400, 0
	v_add_u32_e32 v189, s46, v182
	s_waitcnt vmcnt(2)
	s_barrier
	ds_read_b128 v[130:133], v189 offset:33280
	ds_read_b128 v[146:149], v189 offset:33344
	ds_read_b128 v[200:203], v189 offset:37632
	ds_read_b128 v[204:207], v189 offset:37696
	ds_read_b128 v[212:215], v189 offset:41984
	ds_read_b128 v[216:219], v189 offset:42048
	ds_read_b128 v[224:227], v189 offset:46336
	ds_read_b128 v[228:231], v189 offset:46400
	s_mov_b32 m0, s85
	s_nop 0
	global_load_lds_dwordx4 v253, s[74:75]
	s_add_i32 m0, s85, 0x400
	s_nop 0
	global_load_lds_dwordx4 v253, s[76:77]
	s_add_u32 s74, s74, 0x90000
	s_addc_u32 s75, s75, 0
	s_add_u32 s76, s76, 0x90000
	s_addc_u32 s77, s77, 0
	v_cvt_pk_bf16_f32 v124, v134, v138
	v_cvt_pk_bf16_f32 v125, v136, v140
	v_cvt_pk_bf16_f32 v128, v135, v139
	v_cvt_pk_bf16_f32 v129, v137, v141
	v_cvt_pk_bf16_f32 v114, v246, v152
	v_cvt_pk_bf16_f32 v115, v240, v160
	v_cvt_pk_bf16_f32 v116, v168, v170
	v_cvt_pk_bf16_f32 v117, v242, v244
	v_cvt_pk_bf16_f32 v118, v247, v153
	v_cvt_pk_bf16_f32 v119, v241, v161
	v_cvt_pk_bf16_f32 v120, v169, v171
	v_cvt_pk_bf16_f32 v121, v243, v245
	v_cvt_pk_bf16_f32 v122, v142, v172
	v_cvt_pk_bf16_f32 v123, v144, v174
	v_cvt_pk_bf16_f32 v126, v143, v173
	v_cvt_pk_bf16_f32 v127, v145, v175
	s_waitcnt lgkmcnt(7)
	v_mfma_f32_16x16x32_bf16 v[196:199], v[130:133], v[30:33], v[248:251]
	v_add_f32_e64 v134, v134, v138
	v_add_f32_e64 v135, v135, v139
	v_pk_add_f32 v[136:137], v[136:137], v[140:141]
	s_mul_i32 s46, s16, 0x4100
	v_mfma_f32_16x16x32_bf16 v[130:133], v[130:133], v[38:41], v[248:251]
	s_waitcnt lgkmcnt(5)
	v_mfma_f32_16x16x32_bf16 v[208:211], v[200:203], v[30:33], v[248:251]
	v_mfma_f32_16x16x32_bf16 v[200:203], v[200:203], v[38:41], v[248:251]
	s_waitcnt lgkmcnt(3)
	v_mfma_f32_16x16x32_bf16 v[220:223], v[212:215], v[30:33], v[248:251]
	v_mfma_f32_16x16x32_bf16 v[212:215], v[212:215], v[38:41], v[248:251]
	s_waitcnt lgkmcnt(1)
	v_mfma_f32_16x16x32_bf16 v[232:235], v[224:227], v[30:33], v[248:251]
	v_mfma_f32_16x16x32_bf16 v[224:227], v[224:227], v[38:41], v[248:251]
	v_mfma_f32_16x16x32_bf16 v[196:199], v[146:149], v[18:21], v[196:199]
	v_mfma_f32_16x16x32_bf16 v[130:133], v[146:149], v[22:25], v[130:133]
	v_mfma_f32_16x16x32_bf16 v[146:149], v[204:207], v[18:21], v[208:211]
	v_mfma_f32_16x16x32_bf16 v[200:203], v[204:207], v[22:25], v[200:203]
	v_mfma_f32_16x16x32_bf16 v[204:207], v[216:219], v[18:21], v[220:223]
	v_mfma_f32_16x16x32_bf16 v[208:211], v[216:219], v[22:25], v[212:215]
	s_waitcnt lgkmcnt(0)
	v_mfma_f32_16x16x32_bf16 v[216:219], v[228:231], v[22:25], v[224:227]
	ds_read_b128 v[220:223], v189 offset:33408
	s_nop 1
	ds_read_b128 v[224:227], v189 offset:33472
	v_mfma_f32_16x16x32_bf16 v[212:215], v[228:231], v[18:21], v[232:235]
	s_waitcnt lgkmcnt(1)
	v_mfma_f32_16x16x32_bf16 v[196:199], v[220:223], v[10:13], v[196:199]
	v_mfma_f32_16x16x32_bf16 v[130:133], v[220:223], v[14:17], v[130:133]
	ds_read_b128 v[220:223], v189 offset:37760
	ds_read_b128 v[228:231], v189 offset:37824
	s_waitcnt lgkmcnt(1)
	v_mfma_f32_16x16x32_bf16 v[146:149], v[220:223], v[10:13], v[146:149]
	v_mfma_f32_16x16x32_bf16 v[200:203], v[220:223], v[14:17], v[200:203]
	ds_read_b128 v[220:223], v189 offset:42112
	ds_read_b128 v[232:235], v189 offset:42176
	s_waitcnt lgkmcnt(1)
	v_mfma_f32_16x16x32_bf16 v[204:207], v[220:223], v[10:13], v[204:207]
	v_mfma_f32_16x16x32_bf16 v[208:211], v[220:223], v[14:17], v[208:211]
	ds_read_b128 v[220:223], v189 offset:46464
	ds_read_b128 v[236:239], v189 offset:46528
	v_add_u32_e32 v189, s46, v183
	s_waitcnt lgkmcnt(1)
	v_mfma_f32_16x16x32_bf16 v[212:215], v[220:223], v[10:13], v[212:215]
	v_mfma_f32_16x16x32_bf16 v[216:219], v[220:223], v[14:17], v[216:219]
	v_mfma_f32_16x16x32_bf16 v[220:223], v[224:227], v[6:9], v[130:133]
	s_nop 2
	v_add_f32_e64 v130, v246, v152
	v_add_f32_e64 v131, v247, v153
	v_pk_add_f32 v[132:133], v[240:241], v[160:161]
	v_pk_add_f32 v[152:153], v[168:169], v[170:171]
	v_pk_add_f32 v[156:157], v[242:243], v[244:245]
	v_pk_add_f32 v[158:159], v[142:143], v[172:173]
	v_pk_add_f32 v[160:161], v[144:145], v[174:175]
	v_pk_add_f32 v[130:131], v[130:131], v[132:133]
	v_mfma_f32_16x16x32_bf16 v[142:145], v[232:235], v[2:5], v[204:207]
	v_add_f32_e64 v152, v152, v156
	v_add_f32_e64 v153, v153, v157
	v_pk_add_f32 v[156:157], v[158:159], v[160:161]
	v_pk_add_f32 v[158:159], v[134:135], v[136:137]
	v_mfma_f32_16x16x32_bf16 v[138:141], v[232:235], v[6:9], v[208:211]
	v_add_f32_e64 v150, v150, v130
	v_add_f32_e64 v151, v151, v131
	v_pk_add_f32 v[150:151], v[152:153], v[150:151]
	s_waitcnt lgkmcnt(0)
	v_mfma_f32_16x16x32_bf16 v[134:137], v[236:239], v[2:5], v[212:215]
	v_add_f32_e64 v150, v156, v150
	v_add_f32_e64 v151, v157, v151
	v_pk_add_f32 v[150:151], v[158:159], v[150:151]
	v_mfma_f32_16x16x32_bf16 v[196:199], v[224:227], v[2:5], v[196:199]
	v_mfma_f32_16x16x32_bf16 v[224:227], v[228:231], v[2:5], v[146:149]
	v_mfma_f32_16x16x32_bf16 v[146:149], v[228:231], v[6:9], v[200:203]
	v_mfma_f32_16x16x32_bf16 v[130:133], v[236:239], v[6:9], v[216:219]
	ds_read_b64_tr_b16 v[156:157], v189 offset:0
	ds_read_b64_tr_b16 v[158:159], v189 offset:0x200
	ds_read_b64_tr_b16 v[164:165], v189 offset:0x400
	ds_read_b64_tr_b16 v[166:167], v189 offset:0x600
	ds_read_b64_tr_b16 v[168:169], v189 offset:0x820
	ds_read_b64_tr_b16 v[170:171], v189 offset:0xa20
	ds_read_b64_tr_b16 v[172:173], v189 offset:0xc20
	ds_read_b64_tr_b16 v[174:175], v189 offset:0xe20
	ds_read_b64_tr_b16 v[200:201], v189 offset:0x1040
	ds_read_b64_tr_b16 v[202:203], v189 offset:0x1240
	ds_read_b64_tr_b16 v[204:205], v189 offset:0x1440
	ds_read_b64_tr_b16 v[206:207], v189 offset:0x1640
	s_waitcnt lgkmcnt(4)
; #define SBAR() __builtin_amdgcn_sched_barrier(0)
; #define MFMA16(a, b, c) __builtin_amdgcn_mfma_f32_16x16x32_bf16(a, b, c, 0, 0, 0)
; template <int D0> __device__ __forceinline__ void pv16(f32x4a (&o)[8][2], int vb, const bf16x8 (&pb)[2][2]) {
;     ...
;   const s16x4 a0 = TR(D0, 0, 0), a1 = TR(D0, 0, 1), a2 = TR(D0, 1, 0), a3 = TR(D0, 1, 1), b0 = TR(D0 + 1, 0, 0), b1 = TR(D0 + 1, 0, 1), b2 = TR(D0 + 1, 1, 0), b3 = TR(D0 + 1, 1, 1);
;   const s16x4 c0 = TR(D0 + 2, 0, 0), c1 = TR(D0 + 2, 0, 1), c2 = TR(D0 + 2, 1, 0), c3 = TR(D0 + 2, 1, 1);
;   asm volatile("s_waitcnt lgkmcnt(4)" ::: "memory"); SBAR();
;   o[D0][0] = MFMA16(PK16(a0, a1), pb[0][0], o[D0][0]); o[D0][1] = MFMA16(PK16(a0, a1), pb[0][1], o[D0][1]);
;   o[D0 + 1][0] = MFMA16(PK16(b0, b1), pb[0][0], o[D0 + 1][0]); o[D0 + 1][1] = MFMA16(PK16(b0, b1), pb[0][1], o[D0 + 1][1]);
;   o[D0][0] = MFMA16(PK16(a2, a3), pb[1][0], o[D0][0]); o[D0][1] = MFMA16(PK16(a2, a3), pb[1][1], o[D0][1]);
;   o[D0 + 1][0] = MFMA16(PK16(b2, b3), pb[1][0], o[D0 + 1][0]); o[D0 + 1][1] = MFMA16(PK16(b2, b3), pb[1][1], o[D0 + 1][1]);
;   SBAR();
;   const s16x4 d0 = TR(D0 + 3, 0, 0), d1 = TR(D0 + 3, 0, 1), d2 = TR(D0 + 3, 1, 0), d3 = TR(D0 + 3, 1, 1);
;   asm volatile("s_waitcnt lgkmcnt(4)" ::: "memory"); SBAR();
;   o[D0 + 2][0] = MFMA16(PK16(c0, c1), pb[0][0], o[D0 + 2][0]); o[D0 + 2][1] = MFMA16(PK16(c0, c1), pb[0][1], o[D0 + 2][1]);
;   o[D0 + 2][0] = MFMA16(PK16(c2, c3), pb[1][0], o[D0 + 2][0]); o[D0 + 2][1] = MFMA16(PK16(c2, c3), pb[1][1], o[D0 + 2][1]);
;   asm volatile("s_waitcnt lgkmcnt(0)" ::: "memory"); SBAR();
;   o[D0 + 3][0] = MFMA16(PK16(d0, d1), pb[0][0], o[D0 + 3][0]); o[D0 + 3][1] = MFMA16(PK16(d0, d1), pb[0][1], o[D0 + 3][1]);
;   o[D0 + 3][0] = MFMA16(PK16(d2, d3), pb[1][0], o[D0 + 3][0]); o[D0 + 3][1] = MFMA16(PK16(d2, d3), pb[1][1], o[D0 + 3][1]);
; template <int LDQ, int LDK, int LDO>
; __device__ __forceinline__ void attn_gqa16_body(const bf16* __restrict__ Qb, const bf16* __restrict__ Kh, const bf16* __restrict__ Vh, bf16* __restrict__ Ob, int seq, char* lds, float mref) {
;     ...
;     asm volatile("s_waitcnt vmcnt(0)" ::: "memory");
;     if (t + 2 < NT) HWRITEK(t & 1);
;     if (t + 1 < NT) HWRITEV((t + 1) & 1);
;     HLOADK(t + 3); HLOADV(t + 2);
;     SBAR(); pv16<4>(o, vb, pb); SBAR();
;     if (more) HEXP();
	s_nop 0
	v_mfma_f32_16x16x32_bf16 v[102:105], v[156:159], v[114:117], v[102:105]
	v_mfma_f32_16x16x32_bf16 v[98:101], v[156:159], v[118:121], v[98:101]
	v_mfma_f32_16x16x32_bf16 v[94:97], v[168:171], v[114:117], v[94:97]
	v_exp_f32_e32 v246, v196
	v_mfma_f32_16x16x32_bf16 v[90:93], v[168:171], v[118:121], v[90:93]
	v_exp_f32_e32 v240, v198
	v_mfma_f32_16x16x32_bf16 v[102:105], v[164:167], v[122:125], v[102:105]
	v_exp_f32_e32 v160, v199
	v_mfma_f32_16x16x32_bf16 v[98:101], v[164:167], v[126:129], v[98:101]
	v_exp_f32_e32 v247, v220
	v_mfma_f32_16x16x32_bf16 v[94:97], v[172:175], v[122:125], v[94:97]
	v_exp_f32_e32 v241, v222
	v_mfma_f32_16x16x32_bf16 v[90:93], v[172:175], v[126:129], v[90:93]
	v_exp_f32_e32 v161, v223
	ds_read_b64_tr_b16 v[156:157], v189 offset:0x1860
	ds_read_b64_tr_b16 v[158:159], v189 offset:0x1a60
	ds_read_b64_tr_b16 v[164:165], v189 offset:0x1c60
	ds_read_b64_tr_b16 v[166:167], v189 offset:0x1e60
	s_waitcnt lgkmcnt(4)
	v_mfma_f32_16x16x32_bf16 v[78:81], v[200:203], v[114:117], v[78:81]
	v_exp_f32_e32 v172, v143
	s_waitcnt lgkmcnt(0)
	v_mfma_f32_16x16x32_bf16 v[50:53], v[200:203], v[118:121], v[50:53]
	v_exp_f32_e32 v174, v145
	v_mfma_f32_16x16x32_bf16 v[78:81], v[204:207], v[122:125], v[78:81]
	v_exp_f32_e32 v143, v138
	v_mfma_f32_16x16x32_bf16 v[50:53], v[204:207], v[126:129], v[50:53]
	v_exp_f32_e32 v173, v139
	v_mfma_f32_16x16x32_bf16 v[82:85], v[156:159], v[114:117], v[82:85]
	v_exp_f32_e32 v145, v140
	v_mfma_f32_16x16x32_bf16 v[86:89], v[156:159], v[118:121], v[86:89]
	v_exp_f32_e32 v175, v141
	v_mfma_f32_16x16x32_bf16 v[82:85], v[164:167], v[122:125], v[82:85]
	v_exp_f32_e32 v138, v135
	v_mfma_f32_16x16x32_bf16 v[86:89], v[164:167], v[126:129], v[86:89]
	v_exp_f32_e32 v140, v137
	v_lshl_add_u64 v[152:153], v[162:163], 0, s[14:15]
	v_add_co_u32_e32 v156, vcc, s37, v152
	s_mulk_i32 s16, 0x4400
	s_nop 0
	v_addc_co_u32_e32 v157, vcc, 0, v153, vcc
	v_add_co_u32_e32 v158, vcc, s38, v152
	v_add_u32_e32 v164, s16, v194
	s_nop 0
	v_addc_co_u32_e32 v159, vcc, 0, v153, vcc
	s_waitcnt vmcnt(2)
	ds_write_b128 v164, v[106:109] offset:33280
	ds_write_b128 v164, v[110:113] offset:41984
	global_load_dwordx4 v[106:109], v[156:157], off offset:3072
	global_load_dwordx4 v[110:113], v[158:159], off offset:3072
	ds_read_b64_tr_b16 v[156:157], v189 offset:0x2080
	ds_read_b64_tr_b16 v[158:159], v189 offset:0x2280
	ds_read_b64_tr_b16 v[164:165], v189 offset:0x2480
	ds_read_b64_tr_b16 v[166:167], v189 offset:0x2680
	ds_read_b64_tr_b16 v[200:201], v189 offset:0x28a0
	ds_read_b64_tr_b16 v[202:203], v189 offset:0x2aa0
	ds_read_b64_tr_b16 v[204:205], v189 offset:0x2ca0
	ds_read_b64_tr_b16 v[206:207], v189 offset:0x2ea0
	s_waitcnt lgkmcnt(6)
	s_nop 0
	v_mfma_f32_16x16x32_bf16 v[54:57], v[156:159], v[114:117], v[54:57]
	v_exp_f32_e32 v135, v130
	v_mfma_f32_16x16x32_bf16 v[62:65], v[156:159], v[118:121], v[62:65]
	v_exp_f32_e32 v139, v131
	ds_read_b64_tr_b16 v[156:157], v189 offset:0x30c0
	ds_read_b64_tr_b16 v[158:159], v189 offset:0x32c0
	s_waitcnt lgkmcnt(4)
	v_mfma_f32_16x16x32_bf16 v[58:61], v[200:203], v[114:117], v[58:61]
	v_exp_f32_e32 v137, v132
	v_mfma_f32_16x16x32_bf16 v[70:73], v[200:203], v[118:121], v[70:73]
	v_exp_f32_e32 v141, v133
	ds_read_b64_tr_b16 v[200:201], v189 offset:0x38e0
	ds_read_b64_tr_b16 v[202:203], v189 offset:0x3ae0
	s_waitcnt lgkmcnt(6)
	v_mfma_f32_16x16x32_bf16 v[54:57], v[164:167], v[122:125], v[54:57]
	v_exp_f32_e32 v168, v224
	v_mfma_f32_16x16x32_bf16 v[62:65], v[164:167], v[126:129], v[62:65]
	v_exp_f32_e32 v170, v225
	ds_read_b64_tr_b16 v[164:165], v189 offset:0x34c0
	ds_read_b64_tr_b16 v[166:167], v189 offset:0x36c0
	s_waitcnt lgkmcnt(6)
	v_mfma_f32_16x16x32_bf16 v[58:61], v[204:207], v[122:125], v[58:61]
	v_exp_f32_e32 v169, v146
	v_mfma_f32_16x16x32_bf16 v[70:73], v[204:207], v[126:129], v[70:73]
	v_exp_f32_e32 v171, v147
	ds_read_b64_tr_b16 v[204:205], v189 offset:0x3ce0
	ds_read_b64_tr_b16 v[206:207], v189 offset:0x3ee0
	s_waitcnt lgkmcnt(6)
	v_mfma_f32_16x16x32_bf16 v[42:45], v[156:159], v[114:117], v[42:45]
	v_exp_f32_e32 v152, v197
	v_exp_f32_e32 v134, v134
	v_mfma_f32_16x16x32_bf16 v[46:49], v[156:159], v[118:121], v[46:49]
	v_exp_f32_e32 v153, v221
	v_exp_f32_e32 v136, v136
	s_waitcnt lgkmcnt(4)
	v_mfma_f32_16x16x32_bf16 v[66:69], v[200:203], v[114:117], v[66:69]
	v_exp_f32_e32 v242, v226
	v_mfma_f32_16x16x32_bf16 v[74:77], v[200:203], v[118:121], v[74:77]
	v_exp_f32_e32 v244, v227
	s_waitcnt lgkmcnt(2)
	v_mfma_f32_16x16x32_bf16 v[42:45], v[164:167], v[122:125], v[42:45]
	v_exp_f32_e32 v243, v148
	v_mfma_f32_16x16x32_bf16 v[46:49], v[164:167], v[126:129], v[46:49]
	v_exp_f32_e32 v245, v149
	s_waitcnt lgkmcnt(0)
	v_mfma_f32_16x16x32_bf16 v[66:69], v[204:207], v[122:125], v[66:69]
	v_exp_f32_e32 v142, v142
	v_mfma_f32_16x16x32_bf16 v[74:77], v[204:207], v[126:129], v[74:77]
	v_exp_f32_e32 v144, v144
	s_add_u32 s14, s14, 0x90000
	s_addc_u32 s15, s15, 0
	s_cmp_lg_u32 s14, 0x9120000
	s_mov_b32 s16, s17
	s_cbranch_scc1 .LBB0_650
	v_mov_b32_e32 v156, v240
	v_mov_b32_e32 v157, v241
	v_mov_b32_e32 v158, v246
	v_mov_b32_e32 v159, v247
	v_mov_b32_e32 v164, v242
	v_mov_b32_e32 v165, v243
	v_mov_b32_e32 v166, v244
	v_mov_b32_e32 v167, v245
	s_waitcnt vmcnt(1)
	v_cvt_pk_bf16_f32 v106, v158, v152
	v_cvt_pk_bf16_f32 v107, v156, v160
	v_cvt_pk_bf16_f32 v108, v168, v170
	v_cvt_pk_bf16_f32 v109, v164, v166
	s_waitcnt vmcnt(0)
	v_cvt_pk_bf16_f32 v110, v159, v153
	v_cvt_pk_bf16_f32 v111, v157, v161
	v_cvt_pk_bf16_f32 v112, v169, v171
	v_cvt_pk_bf16_f32 v113, v165, v167
	v_cvt_pk_bf16_f32 v114, v142, v172
	v_cvt_pk_bf16_f32 v115, v144, v174
	v_cvt_pk_bf16_f32 v116, v134, v138
	v_cvt_pk_bf16_f32 v117, v136, v140
	v_cvt_pk_bf16_f32 v118, v143, v173
	v_cvt_pk_bf16_f32 v119, v145, v175
	v_cvt_pk_bf16_f32 v120, v135, v139
	v_cvt_pk_bf16_f32 v121, v137, v141
	s_waitcnt lgkmcnt(0)
	s_barrier
; #define SBAR() __builtin_amdgcn_sched_barrier(0)
; template <int LDQ, int LDK, int LDO>
; __device__ __forceinline__ void attn_gqa16_body(const bf16* __restrict__ Qb, const bf16* __restrict__ Kh, const bf16* __restrict__ Vh, bf16* __restrict__ Ob, int seq, char* lds, float mref) {
;     ...
;   for (int t = 0; t < NT; ++t) {
;     HPACK();
;     __syncthreads();
;     const bool more = t + 1 < NT;
;     if (more) HQK((t + 1) & 1);
;     const int vb = vb0 + (t & 1) * (int)G16_V;
;     SBAR(); pv16<0>(o, vb, pb); SBAR();
	s_mov_b32 m0, s86
	s_nop 0
	global_load_lds_dwordx4 v253, s[74:75]
	s_add_i32 m0, s86, 0x400
	s_nop 0
	global_load_lds_dwordx4 v253, s[76:77]
	ds_read_b128 v[122:125], v182 offset:50688
	ds_read_b128 v[126:129], v182 offset:50752
	ds_read_b128 v[146:149], v182 offset:55040
	ds_read_b128 v[196:199], v182 offset:55104
	ds_read_b128 v[204:207], v182 offset:59392
	ds_read_b128 v[208:211], v182 offset:59456
	ds_read_b128 v[216:219], v182 offset:63744
	ds_read_b128 v[220:223], v182 offset:63808
	s_waitcnt lgkmcnt(7)
	v_mfma_f32_16x16x32_bf16 v[130:133], v[122:125], v[30:33], 0
	v_mov_b32_e32 v190, v168
	v_mov_b32_e32 v191, v158
	v_mov_b32_e32 v192, v170
	v_mfma_f32_16x16x32_bf16 v[122:125], v[122:125], v[38:41], 0
	v_mov_b32_e32 v193, v152
	v_mov_b32_e32 v152, v171
	s_lshl_b32 s8, s8, 12
	s_waitcnt lgkmcnt(5)
	v_mfma_f32_16x16x32_bf16 v[200:203], v[146:149], v[30:33], 0
	s_add_u32 s8, s42, s8
	s_addc_u32 s14, s43, 0
	s_add_u32 s12, s8, s12
	v_mfma_f32_16x16x32_bf16 v[146:149], v[146:149], v[38:41], 0
	s_addc_u32 s13, s14, s13
	s_waitcnt lgkmcnt(3)
	v_mfma_f32_16x16x32_bf16 v[212:215], v[204:207], v[30:33], 0
	s_waitcnt lgkmcnt(1)
	v_mfma_f32_16x16x32_bf16 v[30:33], v[216:219], v[30:33], 0
	v_mfma_f32_16x16x32_bf16 v[130:133], v[126:129], v[18:21], v[130:133]
	v_mfma_f32_16x16x32_bf16 v[122:125], v[126:129], v[22:25], v[122:125]
	v_mfma_f32_16x16x32_bf16 v[126:129], v[196:199], v[18:21], v[200:203]
	v_mfma_f32_16x16x32_bf16 v[146:149], v[196:199], v[22:25], v[146:149]
	v_mfma_f32_16x16x32_bf16 v[196:199], v[208:211], v[18:21], v[212:215]
	s_waitcnt lgkmcnt(0)
	v_mfma_f32_16x16x32_bf16 v[18:21], v[220:223], v[18:21], v[30:33]
	s_nop 0
	v_mov_b32_e32 v213, v156
	v_mov_b32_e32 v212, v164
	v_mov_b32_e32 v214, v166
	ds_read_b128 v[30:33], v182 offset:50816
	v_mfma_f32_16x16x32_bf16 v[204:207], v[204:207], v[38:41], 0
	v_mov_b32_e32 v215, v160
	v_mfma_f32_16x16x32_bf16 v[38:41], v[216:219], v[38:41], 0
	v_mov_b32_e32 v216, v169
	v_mov_b32_e32 v217, v159
	v_mov_b32_e32 v219, v157
	v_mfma_f32_16x16x32_bf16 v[200:203], v[208:211], v[22:25], v[204:207]
	v_mov_b32_e32 v218, v165
	v_mfma_f32_16x16x32_bf16 v[22:25], v[220:223], v[22:25], v[38:41]
	s_nop 2
	ds_read_b128 v[38:41], v182 offset:55168
	ds_read_b128 v[204:207], v182 offset:50880
	s_waitcnt lgkmcnt(2)
	v_mfma_f32_16x16x32_bf16 v[130:133], v[30:33], v[10:13], v[130:133]
	v_mfma_f32_16x16x32_bf16 v[30:33], v[30:33], v[14:17], v[122:125]
	s_nop 2
	ds_read_b128 v[122:125], v182 offset:59520
	ds_read_b128 v[208:211], v182 offset:55232
	s_waitcnt lgkmcnt(3)
	v_mfma_f32_16x16x32_bf16 v[126:129], v[38:41], v[10:13], v[126:129]
	v_mfma_f32_16x16x32_bf16 v[38:41], v[38:41], v[14:17], v[146:149]
	s_nop 2
	ds_read_b128 v[146:149], v182 offset:63872
	ds_read_b128 v[168:171], v182 offset:59584
	ds_read_b128 v[156:159], v182 offset:63936
	s_waitcnt lgkmcnt(4)
	v_mfma_f32_16x16x32_bf16 v[196:199], v[122:125], v[10:13], v[196:199]
	s_waitcnt lgkmcnt(2)
	v_mfma_f32_16x16x32_bf16 v[10:13], v[146:149], v[10:13], v[18:21]
	v_mfma_f32_16x16x32_bf16 v[122:125], v[122:125], v[14:17], v[200:203]
	s_nop 1
	v_mov_b32_e32 v18, v142
	v_mov_b32_e32 v19, v144
	v_mov_b32_e32 v20, v172
	v_mfma_f32_16x16x32_bf16 v[14:17], v[146:149], v[14:17], v[22:25]
	v_mov_b32_e32 v201, v161
	v_mov_b32_e32 v200, v167
	v_mov_b32_e32 v21, v174
	v_mfma_f32_16x16x32_bf16 v[160:163], v[204:207], v[6:9], v[30:33]
	v_add_f32_e64 v24, v190, v192
	v_add_f32_e64 v25, v191, v193
	v_mov_b32_e32 v144, v143
	v_mov_b32_e32 v22, v173
	v_pk_add_f32 v[30:31], v[212:213], v[214:215]
	v_mfma_f32_16x16x32_bf16 v[146:149], v[204:207], v[2:5], v[130:133]
	v_add_f32_e64 v24, v24, v30
	v_add_f32_e64 v25, v25, v31
	v_mov_b32_e32 v23, v175
	v_pk_add_f32 v[32:33], v[216:217], v[152:153]
	v_mfma_f32_16x16x32_bf16 v[164:167], v[208:211], v[2:5], v[126:129]
	v_add_f32_e64 v144, v144, v22
	v_add_f32_e64 v145, v145, v23
	v_add_f32_e32 v130, v134, v138
	v_add_f32_e32 v132, v136, v140
	v_mfma_f32_16x16x32_bf16 v[172:175], v[208:211], v[6:9], v[38:41]
	v_add_f32_e64 v126, v18, v20
	v_add_f32_e64 v127, v19, v21
	s_nop 0
	v_pk_add_f32 v[38:39], v[218:219], v[200:201]
	s_waitcnt lgkmcnt(1)
	v_mfma_f32_16x16x32_bf16 v[196:199], v[168:171], v[2:5], v[196:199]
	v_add_f32_e64 v142, v32, v38
	v_add_f32_e64 v143, v33, v39
	s_waitcnt lgkmcnt(0)
	v_mfma_f32_16x16x32_bf16 v[200:203], v[156:159], v[2:5], v[10:13]
	v_add_f32_e64 v2, v150, v25
	v_add_f32_e64 v3, v151, v24
	v_pk_add_f32 v[128:129], v[24:25], v[2:3]
	v_mfma_f32_16x16x32_bf16 v[168:171], v[168:171], v[6:9], v[122:125]
	s_nop 2
	v_add_f32_e32 v122, v135, v139
	v_add_f32_e32 v124, v137, v141
	v_mfma_f32_16x16x32_bf16 v[134:137], v[156:159], v[6:9], v[14:17]
	ds_read_b64_tr_b16 v[2:3], v183 offset:0
	ds_read_b64_tr_b16 v[4:5], v183 offset:0x200
	ds_read_b64_tr_b16 v[6:7], v183 offset:0x400
	ds_read_b64_tr_b16 v[8:9], v183 offset:0x600
	ds_read_b64_tr_b16 v[10:11], v183 offset:0x820
	ds_read_b64_tr_b16 v[12:13], v183 offset:0xa20
	ds_read_b64_tr_b16 v[14:15], v183 offset:0xc20
	ds_read_b64_tr_b16 v[16:17], v183 offset:0xe20
	ds_read_b64_tr_b16 v[18:19], v183 offset:0x1040
	ds_read_b64_tr_b16 v[20:21], v183 offset:0x1240
	ds_read_b64_tr_b16 v[22:23], v183 offset:0x1440
	ds_read_b64_tr_b16 v[24:25], v183 offset:0x1640
	s_waitcnt lgkmcnt(4)
	s_nop 0
	v_mfma_f32_16x16x32_bf16 v[30:33], v[2:5], v[106:109], v[102:105]
	v_mfma_f32_16x16x32_bf16 v[38:41], v[2:5], v[110:113], v[98:101]
	v_mfma_f32_16x16x32_bf16 v[94:97], v[10:13], v[106:109], v[94:97]
	v_mfma_f32_16x16x32_bf16 v[10:13], v[10:13], v[110:113], v[90:93]
	v_mfma_f32_16x16x32_bf16 v[2:5], v[6:9], v[114:117], v[30:33]
	v_mfma_f32_16x16x32_bf16 v[6:9], v[6:9], v[118:121], v[38:41]
	v_mfma_f32_16x16x32_bf16 v[38:41], v[14:17], v[114:117], v[94:97]
	v_mfma_f32_16x16x32_bf16 v[90:93], v[14:17], v[118:121], v[10:13]
	ds_read_b64_tr_b16 v[14:15], v183 offset:0x1860
	ds_read_b64_tr_b16 v[16:17], v183 offset:0x1a60
	ds_read_b64_tr_b16 v[30:31], v183 offset:0x1c60
	ds_read_b64_tr_b16 v[32:33], v183 offset:0x1e60
	s_waitcnt lgkmcnt(4)
; #define SBAR() __builtin_amdgcn_sched_barrier(0)
; #define MFMA16(a, b, c) __builtin_amdgcn_mfma_f32_16x16x32_bf16(a, b, c, 0, 0, 0)
; template <int D0> __device__ __forceinline__ void pv16(f32x4a (&o)[8][2], int vb, const bf16x8 (&pb)[2][2]) {
;     ...
;   const s16x4 a0 = TR(D0, 0, 0), a1 = TR(D0, 0, 1), a2 = TR(D0, 1, 0), a3 = TR(D0, 1, 1), b0 = TR(D0 + 1, 0, 0), b1 = TR(D0 + 1, 0, 1), b2 = TR(D0 + 1, 1, 0), b3 = TR(D0 + 1, 1, 1);
;   const s16x4 c0 = TR(D0 + 2, 0, 0), c1 = TR(D0 + 2, 0, 1), c2 = TR(D0 + 2, 1, 0), c3 = TR(D0 + 2, 1, 1);
;   asm volatile("s_waitcnt lgkmcnt(4)" ::: "memory"); SBAR();
;   o[D0][0] = MFMA16(PK16(a0, a1), pb[0][0], o[D0][0]); o[D0][1] = MFMA16(PK16(a0, a1), pb[0][1], o[D0][1]);
;   o[D0 + 1][0] = MFMA16(PK16(b0, b1), pb[0][0], o[D0 + 1][0]); o[D0 + 1][1] = MFMA16(PK16(b0, b1), pb[0][1], o[D0 + 1][1]);
;   o[D0][0] = MFMA16(PK16(a2, a3), pb[1][0], o[D0][0]); o[D0][1] = MFMA16(PK16(a2, a3), pb[1][1], o[D0][1]);
;   o[D0 + 1][0] = MFMA16(PK16(b2, b3), pb[1][0], o[D0 + 1][0]); o[D0 + 1][1] = MFMA16(PK16(b2, b3), pb[1][1], o[D0 + 1][1]);
;   SBAR();
;   const s16x4 d0 = TR(D0 + 3, 0, 0), d1 = TR(D0 + 3, 0, 1), d2 = TR(D0 + 3, 1, 0), d3 = TR(D0 + 3, 1, 1);
;   asm volatile("s_waitcnt lgkmcnt(4)" ::: "memory"); SBAR();
;   o[D0 + 2][0] = MFMA16(PK16(c0, c1), pb[0][0], o[D0 + 2][0]); o[D0 + 2][1] = MFMA16(PK16(c0, c1), pb[0][1], o[D0 + 2][1]);
;   o[D0 + 2][0] = MFMA16(PK16(c2, c3), pb[1][0], o[D0 + 2][0]); o[D0 + 2][1] = MFMA16(PK16(c2, c3), pb[1][1], o[D0 + 2][1]);
;   asm volatile("s_waitcnt lgkmcnt(0)" ::: "memory"); SBAR();
;   o[D0 + 3][0] = MFMA16(PK16(d0, d1), pb[0][0], o[D0 + 3][0]); o[D0 + 3][1] = MFMA16(PK16(d0, d1), pb[0][1], o[D0 + 3][1]);
;   o[D0 + 3][0] = MFMA16(PK16(d2, d3), pb[1][0], o[D0 + 3][0]); o[D0 + 3][1] = MFMA16(PK16(d2, d3), pb[1][1], o[D0 + 3][1]);
	v_mfma_f32_16x16x32_bf16 v[10:13], v[18:21], v[106:109], v[78:81]
	s_waitcnt lgkmcnt(0)
	v_mfma_f32_16x16x32_bf16 v[18:21], v[18:21], v[110:113], v[50:53]
	v_mfma_f32_16x16x32_bf16 v[10:13], v[22:25], v[114:117], v[10:13]
	v_mfma_f32_16x16x32_bf16 v[22:25], v[22:25], v[118:121], v[18:21]
	v_mfma_f32_16x16x32_bf16 v[18:21], v[14:17], v[106:109], v[82:85]
	v_mfma_f32_16x16x32_bf16 v[50:53], v[14:17], v[110:113], v[86:89]
	v_mfma_f32_16x16x32_bf16 v[14:17], v[30:33], v[114:117], v[18:21]
	v_mfma_f32_16x16x32_bf16 v[18:21], v[30:33], v[118:121], v[50:53]
	s_waitcnt vmcnt(0)
	s_waitcnt vmcnt(1)
	s_waitcnt vmcnt(0)
	ds_read_b64_tr_b16 v[26:27], v183 offset:0x2080
	ds_read_b64_tr_b16 v[28:29], v183 offset:0x2280
	ds_read_b64_tr_b16 v[30:31], v183 offset:0x2480
	ds_read_b64_tr_b16 v[32:33], v183 offset:0x2680
	ds_read_b64_tr_b16 v[34:35], v183 offset:0x28a0
	ds_read_b64_tr_b16 v[36:37], v183 offset:0x2aa0
	ds_read_b64_tr_b16 v[78:79], v183 offset:0x2ca0
	ds_read_b64_tr_b16 v[80:81], v183 offset:0x2ea0
	ds_read_b64_tr_b16 v[82:83], v183 offset:0x30c0
	ds_read_b64_tr_b16 v[84:85], v183 offset:0x32c0
	ds_read_b64_tr_b16 v[86:87], v183 offset:0x34c0
	ds_read_b64_tr_b16 v[88:89], v183 offset:0x36c0
	s_waitcnt lgkmcnt(4)
	s_nop 0
	v_mfma_f32_16x16x32_bf16 v[50:53], v[26:29], v[106:109], v[54:57]
	v_mfma_f32_16x16x32_bf16 v[26:29], v[26:29], v[110:113], v[62:65]
	v_mfma_f32_16x16x32_bf16 v[58:61], v[34:37], v[106:109], v[58:61]
	v_mfma_f32_16x16x32_bf16 v[34:37], v[34:37], v[110:113], v[70:73]
	v_mfma_f32_16x16x32_bf16 v[50:53], v[30:33], v[114:117], v[50:53]
	v_mfma_f32_16x16x32_bf16 v[54:57], v[30:33], v[118:121], v[26:29]
	v_mfma_f32_16x16x32_bf16 v[70:73], v[78:81], v[114:117], v[58:61]
	v_mfma_f32_16x16x32_bf16 v[78:81], v[78:81], v[118:121], v[34:37]
	ds_read_b64_tr_b16 v[30:31], v183 offset:0x38e0
	ds_read_b64_tr_b16 v[32:33], v183 offset:0x3ae0
	ds_read_b64_tr_b16 v[34:35], v183 offset:0x3ce0
	ds_read_b64_tr_b16 v[36:37], v183 offset:0x3ee0
	s_waitcnt lgkmcnt(4)
	v_mfma_f32_16x16x32_bf16 v[26:29], v[82:85], v[106:109], v[42:45]
	s_waitcnt lgkmcnt(0)
	v_mfma_f32_16x16x32_bf16 v[42:45], v[82:85], v[110:113], v[46:49]
	v_mfma_f32_16x16x32_bf16 v[26:29], v[86:89], v[114:117], v[26:29]
	v_mfma_f32_16x16x32_bf16 v[58:61], v[86:89], v[118:121], v[42:45]
	v_mfma_f32_16x16x32_bf16 v[42:45], v[30:33], v[106:109], v[66:69]
	v_mfma_f32_16x16x32_bf16 v[46:49], v[30:33], v[110:113], v[74:77]
	v_mfma_f32_16x16x32_bf16 v[30:33], v[34:37], v[114:117], v[42:45]
	v_mfma_f32_16x16x32_bf16 v[62:65], v[34:37], v[118:121], v[46:49]
	s_nop 4
	v_add_f32_e32 v42, v186, v196
	v_exp_f32_e32 v116, v42
	v_add_f32_e32 v42, v186, v197
	v_exp_f32_e32 v117, v42
	v_add_f32_e32 v42, v186, v198
	v_exp_f32_e32 v118, v42
	v_add_f32_e32 v42, v186, v199
	v_exp_f32_e32 v119, v42
	v_add_f32_e32 v42, v186, v168
	v_add_f32_e32 v34, v186, v146
	v_exp_f32_e32 v98, v42
	v_add_f32_e32 v42, v186, v169
	v_exp_f32_e32 v131, v34
	v_add_f32_e32 v34, v186, v147
	v_exp_f32_e32 v99, v42
	v_add_f32_e32 v42, v186, v170
	v_exp_f32_e32 v133, v34
	v_add_f32_e32 v34, v186, v148
	v_exp_f32_e32 v100, v42
	v_add_f32_e32 v42, v186, v171
	v_exp_f32_e32 v74, v34
	v_add_f32_e32 v34, v186, v149
	v_exp_f32_e32 v101, v42
	v_add_f32_e32 v42, v186, v200
	v_exp_f32_e32 v129, v34
	v_add_f32_e32 v34, v186, v160
	v_exp_f32_e32 v120, v42
	v_add_f32_e32 v42, v186, v201
	v_exp_f32_e32 v123, v34
	v_add_f32_e32 v34, v186, v161
	v_exp_f32_e32 v121, v42
	v_add_f32_e32 v42, v186, v202
	v_exp_f32_e32 v125, v34
	v_add_f32_e32 v34, v186, v162
	v_exp_f32_e32 v75, v42
	v_add_f32_e32 v42, v186, v203
	v_exp_f32_e32 v76, v34
	v_add_f32_e32 v34, v186, v163
	v_exp_f32_e32 v77, v42
	v_add_f32_e32 v42, v186, v134
	v_exp_f32_e32 v87, v34
	v_add_f32_e32 v34, v186, v164
	v_exp_f32_e32 v102, v42
	v_add_f32_e32 v42, v186, v135
	v_exp_f32_e32 v66, v34
	v_add_f32_e32 v34, v186, v165
	v_exp_f32_e32 v103, v42
	v_add_f32_e32 v42, v186, v136
	v_exp_f32_e32 v68, v34
	v_add_f32_e32 v34, v186, v166
	v_exp_f32_e32 v43, v42
	v_exp_f32_e32 v67, v34
	v_add_f32_e32 v34, v186, v167
	v_add_f32_e32 v35, v186, v173
	v_exp_f32_e32 v69, v34
	v_add_f32_e32 v34, v186, v172
	v_exp_f32_e32 v36, v35
	v_add_f32_e32 v35, v186, v174
	v_add_f32_e32 v37, v186, v175
	v_add_f32_e32 v42, v186, v137
	v_exp_f32_e32 v34, v34
	v_exp_f32_e32 v35, v35
	v_exp_f32_e32 v37, v37
	v_exp_f32_e32 v45, v42
	v_add_f32_e32 v42, v143, v151
	v_pk_add_f32 v[48:49], v[144:145], v[144:145] op_sel:[0,1] op_sel_hi:[1,0]
	v_pk_add_f32 v[84:85], v[142:143], v[42:43] op_sel_hi:[1,0]
	v_mov_b32_e32 v49, v76
	v_mov_b32_e32 v85, v87
	v_pk_add_f32 v[46:47], v[122:123], v[124:125]
	v_pk_add_f32 v[48:49], v[48:49], v[84:85]
	v_add_f32_e32 v42, v98, v99
	v_pk_add_f32 v[46:47], v[46:47], v[48:49]
	v_pk_add_f32 v[48:49], v[34:35], v[36:37]
	v_pk_add_f32 v[46:47], v[46:47], v[46:47] op_sel:[0,1] op_sel_hi:[1,0]
	v_pk_add_f32 v[48:49], v[48:49], v[48:49] op_sel:[0,1] op_sel_hi:[1,0]
	v_add_f32_e32 v44, v100, v101
	v_mov_b32_e32 v47, v102
	v_mov_b32_e32 v49, v103
	v_pk_add_f32 v[46:47], v[46:47], v[48:49]
	v_pk_add_f32 v[48:49], v[42:43], v[44:45]
	v_cvt_pk_bf16_f32 v82, v131, v133
	v_cvt_pk_bf16_f32 v83, v74, v129
	v_cvt_pk_bf16_f32 v84, v66, v68
	v_cvt_pk_bf16_f32 v85, v67, v69
	v_cvt_pk_bf16_f32 v86, v123, v125
	s_nop 0
	v_pk_add_f32 v[46:47], v[46:47], v[48:49]
	v_pk_add_f32 v[48:49], v[126:127], v[126:127] op_sel:[0,1] op_sel_hi:[1,0]
	v_add_f32_e32 v122, v46, v47
	v_mov_b32_e32 v49, v74
	v_pk_add_f32 v[46:47], v[130:131], v[132:133]
	v_pk_add_f32 v[48:49], v[48:49], v[128:129]
	v_cvt_pk_bf16_f32 v87, v76, v87
	v_cvt_pk_bf16_f32 v88, v34, v36
	v_cvt_pk_bf16_f32 v89, v35, v37
	v_cvt_pk_bf16_f32 v94, v116, v117
	v_cvt_pk_bf16_f32 v95, v118, v119
	s_nop 0
	v_pk_add_f32 v[114:115], v[46:47], v[48:49]
	v_cvt_pk_bf16_f32 v96, v120, v121
	v_cvt_pk_bf16_f32 v97, v75, v77
	v_cvt_pk_bf16_f32 v98, v98, v99
	v_cvt_pk_bf16_f32 v99, v100, v101
	v_cvt_pk_bf16_f32 v100, v102, v103
	v_cvt_pk_bf16_f32 v101, v43, v45
	s_waitcnt lgkmcnt(0)
	s_barrier
; #define SBAR() __builtin_amdgcn_sched_barrier(0)
; #define MFMA16(a, b, c) __builtin_amdgcn_mfma_f32_16x16x32_bf16(a, b, c, 0, 0, 0)
; template <int D0> __device__ __forceinline__ void pv16(f32x4a (&o)[8][2], int vb, const bf16x8 (&pb)[2][2]) {
;     ...
;   const s16x4 a0 = TR(D0, 0, 0), a1 = TR(D0, 0, 1), a2 = TR(D0, 1, 0), a3 = TR(D0, 1, 1), b0 = TR(D0 + 1, 0, 0), b1 = TR(D0 + 1, 0, 1), b2 = TR(D0 + 1, 1, 0), b3 = TR(D0 + 1, 1, 1);
;   const s16x4 c0 = TR(D0 + 2, 0, 0), c1 = TR(D0 + 2, 0, 1), c2 = TR(D0 + 2, 1, 0), c3 = TR(D0 + 2, 1, 1);
;   asm volatile("s_waitcnt lgkmcnt(4)" ::: "memory"); SBAR();
;   o[D0][0] = MFMA16(PK16(a0, a1), pb[0][0], o[D0][0]); o[D0][1] = MFMA16(PK16(a0, a1), pb[0][1], o[D0][1]);
;   o[D0 + 1][0] = MFMA16(PK16(b0, b1), pb[0][0], o[D0 + 1][0]); o[D0 + 1][1] = MFMA16(PK16(b0, b1), pb[0][1], o[D0 + 1][1]);
;   o[D0][0] = MFMA16(PK16(a2, a3), pb[1][0], o[D0][0]); o[D0][1] = MFMA16(PK16(a2, a3), pb[1][1], o[D0][1]);
;   o[D0 + 1][0] = MFMA16(PK16(b2, b3), pb[1][0], o[D0 + 1][0]); o[D0 + 1][1] = MFMA16(PK16(b2, b3), pb[1][1], o[D0 + 1][1]);
;   SBAR();
;   const s16x4 d0 = TR(D0 + 3, 0, 0), d1 = TR(D0 + 3, 0, 1), d2 = TR(D0 + 3, 1, 0), d3 = TR(D0 + 3, 1, 1);
;   asm volatile("s_waitcnt lgkmcnt(4)" ::: "memory"); SBAR();
;   o[D0 + 2][0] = MFMA16(PK16(c0, c1), pb[0][0], o[D0 + 2][0]); o[D0 + 2][1] = MFMA16(PK16(c0, c1), pb[0][1], o[D0 + 2][1]);
;   o[D0 + 2][0] = MFMA16(PK16(c2, c3), pb[1][0], o[D0 + 2][0]); o[D0 + 2][1] = MFMA16(PK16(c2, c3), pb[1][1], o[D0 + 2][1]);
;   asm volatile("s_waitcnt lgkmcnt(0)" ::: "memory"); SBAR();
;   o[D0 + 3][0] = MFMA16(PK16(d0, d1), pb[0][0], o[D0 + 3][0]); o[D0 + 3][1] = MFMA16(PK16(d0, d1), pb[0][1], o[D0 + 3][1]);
;   o[D0 + 3][0] = MFMA16(PK16(d2, d3), pb[1][0], o[D0 + 3][0]); o[D0 + 3][1] = MFMA16(PK16(d2, d3), pb[1][1], o[D0 + 3][1]);
; template <int LDQ, int LDK, int LDO>
; __device__ __forceinline__ void attn_gqa16_body(const bf16* __restrict__ Qb, const bf16* __restrict__ Kh, const bf16* __restrict__ Vh, bf16* __restrict__ Ob, int seq, char* lds, float mref) {
;     ...
;   __builtin_amdgcn_s_setprio(0);
;   ls0 += __shfl_xor(ls0, 16); ls0 += __shfl_xor(ls0, 32); ls1 += __shfl_xor(ls1, 16); ls1 += __shfl_xor(ls1, 32);
;   const float rl[2] = {__builtin_amdgcn_rcpf(ls0), __builtin_amdgcn_rcpf(ls1)};
	ds_read_b64_tr_b16 v[34:35], v184 offset:0
	ds_read_b64_tr_b16 v[36:37], v184 offset:0x200
	ds_read_b64_tr_b16 v[42:43], v184 offset:0x400
	ds_read_b64_tr_b16 v[44:45], v184 offset:0x600
	ds_read_b64_tr_b16 v[46:47], v184 offset:0x820
	ds_read_b64_tr_b16 v[48:49], v184 offset:0xa20
	ds_read_b64_tr_b16 v[102:103], v184 offset:0xc20
	ds_read_b64_tr_b16 v[104:105], v184 offset:0xe20
	ds_read_b64_tr_b16 v[106:107], v184 offset:0x1040
	ds_read_b64_tr_b16 v[108:109], v184 offset:0x1240
	ds_read_b64_tr_b16 v[110:111], v184 offset:0x1440
	ds_read_b64_tr_b16 v[112:113], v184 offset:0x1640
	s_waitcnt lgkmcnt(4)
	s_nop 0
	v_mfma_f32_16x16x32_bf16 v[2:5], v[34:37], v[82:85], v[2:5]
	v_mfma_f32_16x16x32_bf16 v[6:9], v[34:37], v[86:89], v[6:9]
	v_mfma_f32_16x16x32_bf16 v[34:37], v[46:49], v[82:85], v[38:41]
	v_mfma_f32_16x16x32_bf16 v[46:49], v[46:49], v[86:89], v[90:93]
	v_mfma_f32_16x16x32_bf16 v[38:41], v[42:45], v[94:97], v[2:5]
	v_mfma_f32_16x16x32_bf16 v[6:9], v[42:45], v[98:101], v[6:9]
	v_mfma_f32_16x16x32_bf16 v[34:37], v[102:105], v[94:97], v[34:37]
	v_mfma_f32_16x16x32_bf16 v[2:5], v[102:105], v[98:101], v[46:49]
	ds_read_b64_tr_b16 v[46:47], v184 offset:0x1860
	ds_read_b64_tr_b16 v[48:49], v184 offset:0x1a60
	ds_read_b64_tr_b16 v[90:91], v184 offset:0x1c60
	ds_read_b64_tr_b16 v[92:93], v184 offset:0x1e60
	s_waitcnt lgkmcnt(4)
	v_mfma_f32_16x16x32_bf16 v[10:13], v[106:109], v[82:85], v[10:13]
	s_waitcnt lgkmcnt(0)
	v_mfma_f32_16x16x32_bf16 v[22:25], v[106:109], v[86:89], v[22:25]
	v_mfma_f32_16x16x32_bf16 v[42:45], v[110:113], v[94:97], v[10:13]
	v_mfma_f32_16x16x32_bf16 v[10:13], v[110:113], v[98:101], v[22:25]
	v_mfma_f32_16x16x32_bf16 v[14:17], v[46:49], v[82:85], v[14:17]
	v_mfma_f32_16x16x32_bf16 v[18:21], v[46:49], v[86:89], v[18:21]
	v_mfma_f32_16x16x32_bf16 v[46:49], v[90:93], v[94:97], v[14:17]
	v_mfma_f32_16x16x32_bf16 v[14:17], v[90:93], v[98:101], v[18:21]
	s_waitcnt vmcnt(0)
	ds_read_b64_tr_b16 v[18:19], v184 offset:0x2080
	ds_read_b64_tr_b16 v[20:21], v184 offset:0x2280
	ds_read_b64_tr_b16 v[22:23], v184 offset:0x2480
	ds_read_b64_tr_b16 v[24:25], v184 offset:0x2680
	ds_read_b64_tr_b16 v[90:91], v184 offset:0x28a0
	ds_read_b64_tr_b16 v[92:93], v184 offset:0x2aa0
	ds_read_b64_tr_b16 v[102:103], v184 offset:0x2ca0
	ds_read_b64_tr_b16 v[104:105], v184 offset:0x2ea0
	ds_read_b64_tr_b16 v[106:107], v184 offset:0x30c0
	ds_read_b64_tr_b16 v[108:109], v184 offset:0x32c0
	ds_read_b64_tr_b16 v[110:111], v184 offset:0x34c0
	ds_read_b64_tr_b16 v[112:113], v184 offset:0x36c0
	s_waitcnt lgkmcnt(4)
	s_nop 5
	v_mfma_f32_16x16x32_bf16 v[50:53], v[18:21], v[82:85], v[50:53]
	v_mfma_f32_16x16x32_bf16 v[18:21], v[18:21], v[86:89], v[54:57]
	v_mfma_f32_16x16x32_bf16 v[70:73], v[90:93], v[82:85], v[70:73]
	v_mfma_f32_16x16x32_bf16 v[78:81], v[90:93], v[86:89], v[78:81]
	v_mfma_f32_16x16x32_bf16 v[54:57], v[22:25], v[94:97], v[50:53]
	v_mfma_f32_16x16x32_bf16 v[22:25], v[22:25], v[98:101], v[18:21]
	v_mfma_f32_16x16x32_bf16 v[50:53], v[102:105], v[94:97], v[70:73]
	v_mfma_f32_16x16x32_bf16 v[18:21], v[102:105], v[98:101], v[78:81]
	ds_read_b64_tr_b16 v[70:71], v184 offset:0x38e0
	ds_read_b64_tr_b16 v[72:73], v184 offset:0x3ae0
	ds_read_b64_tr_b16 v[78:79], v184 offset:0x3ce0
	ds_read_b64_tr_b16 v[80:81], v184 offset:0x3ee0
	s_waitcnt lgkmcnt(4)
	v_mfma_f32_16x16x32_bf16 v[26:29], v[106:109], v[82:85], v[26:29]
	s_waitcnt lgkmcnt(0)
	v_mfma_f32_16x16x32_bf16 v[90:93], v[106:109], v[86:89], v[58:61]
	v_mfma_f32_16x16x32_bf16 v[58:61], v[110:113], v[94:97], v[26:29]
	v_mfma_f32_16x16x32_bf16 v[26:29], v[110:113], v[98:101], v[90:93]
	v_mfma_f32_16x16x32_bf16 v[30:33], v[70:73], v[82:85], v[30:33]
	v_mfma_f32_16x16x32_bf16 v[70:73], v[70:73], v[86:89], v[62:65]
	v_mfma_f32_16x16x32_bf16 v[62:65], v[78:81], v[94:97], v[30:33]
	v_mfma_f32_16x16x32_bf16 v[30:33], v[78:81], v[98:101], v[70:73]
	v_add_f32_e64 v66, v66, v68
	v_add_f32_e64 v67, v67, v69
	v_pk_add_f32 v[68:69], v[114:115], v[114:115] op_sel:[0,1] op_sel_hi:[1,0]
	v_pk_add_f32 v[66:67], v[66:67], v[66:67] op_sel:[0,1] op_sel_hi:[1,0]
	v_add_f32_e32 v74, v116, v117
	v_add_f32_e32 v76, v118, v119
	v_mov_b32_e32 v69, v120
	v_mov_b32_e32 v67, v121
	v_pk_add_f32 v[66:67], v[68:69], v[66:67]
	v_pk_add_f32 v[68:69], v[74:75], v[76:77]
	s_nop 0
	v_pk_add_f32 v[66:67], v[66:67], v[68:69]
	s_nop 0
	v_add_f32_e32 v66, v66, v67
	s_setprio 0
	ds_bpermute_b32 v67, v177, v66
	ds_bpermute_b32 v68, v177, v122
	v_mov_b32_e32 v70, v185
	s_waitcnt lgkmcnt(1)
	v_add_f32_e32 v66, v66, v67
	s_waitcnt lgkmcnt(0)
	v_add_f32_e32 v67, v122, v68
	ds_bpermute_b32 v68, v188, v66
	ds_bpermute_b32 v69, v188, v67
	s_waitcnt lgkmcnt(1)
	v_add_f32_e32 v66, v66, v68
	s_waitcnt lgkmcnt(0)
	v_add_f32_e32 v67, v67, v69
	v_rcp_f32_e32 v68, v66
	v_rcp_f32_e32 v66, v67
	v_mov_b32_e32 v67, v176
	v_mov_b32_e32 v69, v180
	s_branch .LBB0_641
